# speedup vs baseline: 1.0062x; 1.0057x over previous
.LBB2_116:
	s_waitcnt vmcnt(0)
	v_and_b32_e32 v115, 15, v110
	v_lshlrev_b32_e32 v122, 4, v110
	v_mov_b32_e32 v23, 0
	v_mov_b32_e32 v123, v23
	v_or_b32_e32 v0, s33, v115
	v_lshl_add_u64 v[20:21], s[16:17], 0, v[122:123]
	s_mov_b32 s0, 0x4d000
	v_ashrrev_i32_e32 v1, 31, v0
	v_add_co_u32_e32 v36, vcc, s0, v20
	v_lshlrev_b64 v[0:1], 7, v[0:1]
	s_nop 0
	v_addc_co_u32_e32 v37, vcc, 0, v21, vcc
	s_mov_b32 s0, 0x4c000
	v_lshl_add_u64 v[4:5], s[28:29], 0, v[0:1]
	v_lshlrev_b32_e32 v22, 3, v107
	v_add_co_u32_e32 v54, vcc, s0, v20
	v_lshl_add_u64 v[12:13], v[4:5], 0, v[22:23]
	s_nop 0
	v_addc_co_u32_e32 v55, vcc, 0, v21, vcc
	global_load_dwordx4 v[0:3], v[36:37], off offset:-4096
	global_load_dwordx2 v[4:5], v[12:13], off
	global_load_dwordx2 v[6:7], v[12:13], off offset:32
	global_load_dwordx4 v[8:11], v[36:37], off
	global_load_dwordx2 v[24:25], v[12:13], off offset:64
	global_load_dwordx2 v[26:27], v[12:13], off offset:96
	v_lshlrev_b32_e32 v22, 4, v107
	global_load_dwordx4 v[12:15], v[54:55], off offset:2048
	s_mov_b32 s0, 0x3f200000
	s_waitcnt vmcnt(3)
	v_mfma_f32_16x16x32_f16 v[28:31], v[8:11], v[4:7], v[42:45]
	global_load_dwordx4 v[8:11], v[54:55], off offset:1024
	s_waitcnt vmcnt(1)
	v_mfma_f32_16x16x32_f16 v[16:19], v[12:15], v[4:7], v[46:49]
	global_load_dwordx4 v[12:15], v[36:37], off offset:2048
	v_mfma_f32_16x16x32_f16 v[0:3], v[0:3], v[4:7], v[50:53]
	s_waitcnt vmcnt(0)
	v_mfma_f32_16x16x32_f16 v[32:35], v[12:15], v[4:7], v[38:41]
	global_load_dwordx4 v[4:7], v[54:55], off offset:3072
	v_mfma_f32_16x16x32_f16 v[12:15], v[8:11], v[24:27], v[0:3]
	s_nop 3
	global_load_dwordx4 v[0:3], v[36:37], off offset:1024
	s_waitcnt vmcnt(1)
	v_mfma_f32_16x16x32_f16 v[8:11], v[4:7], v[24:27], v[16:19]
	global_load_dwordx4 v[36:39], v[36:37], off offset:3072
	s_nop 1
	global_load_dwordx4 v[16:19], v22, s[18:19]
	global_load_dwordx4 v[200:203], v22, s[18:19] offset:64
	global_load_dwordx4 v[204:207], v22, s[18:19] offset:128
	global_load_dwordx4 v[208:211], v22, s[18:19] offset:192
	s_waitcnt vmcnt(5)
	v_mfma_f32_16x16x32_f16 v[4:7], v[0:3], v[24:27], v[28:31]
	s_waitcnt vmcnt(4)
	v_mfma_f32_16x16x32_f16 v[0:3], v[36:39], v[24:27], v[32:35]
	s_waitcnt vmcnt(0)
	v_add_f32_e32 v24, v12, v16
	v_cmp_nlt_f32_e64 s[0:1], |v24|, s0
	s_and_saveexec_b64 s[2:3], s[0:1]
	s_xor_b64 s[0:1], exec, s[2:3]
	s_cbranch_execz .LBB2_118
	v_add_f32_e64 v12, |v24|, |v24|
	v_mul_f32_e32 v16, 0x3fb8aa3b, v12
	s_mov_b32 s2, 0x3fb8aa3b
	v_rndne_f32_e32 v25, v16
	v_sub_f32_e32 v26, v16, v25
	v_fma_f32 v16, v12, s2, -v16
	v_fmamk_f32 v16, v12, 0x32a5705f, v16
	v_add_f32_e32 v16, v26, v16
	v_exp_f32_e32 v16, v16
	v_cvt_i32_f32_e32 v25, v25
	s_mov_b32 s2, 0xc2ce8ed0
	v_cmp_ngt_f32_e32 vcc, s2, v12
	s_mov_b32 s2, 0x42b17218
	v_ldexp_f32 v16, v16, v25
	v_cndmask_b32_e32 v16, 0, v16, vcc
	v_mov_b32_e32 v25, 0x7f800000
	v_cmp_nlt_f32_e32 vcc, s2, v12
	s_nop 1
	v_cndmask_b32_e32 v12, v25, v16, vcc
	v_add_f32_e32 v12, 1.0, v12
	v_rcp_f32_e32 v12, v12
	s_nop 0
	v_fma_f32 v25, v12, -2.0, 1.0

.LBB2_130:
	s_or_saveexec_b64 s[0:1], s[0:1]
	v_lshl_add_u64 v[16:17], s[18:19], 0, v[22:23]
	s_xor_b64 exec, exec, s[0:1]
	v_mul_f32_e32 v12, v19, v19
	v_mov_b32_e32 v13, 0x3ca908c9
	v_fmac_f32_e32 v13, 0xbbbac73d, v12
	v_fmaak_f32 v13, v12, v13, 0xbd5c1c4e
	v_fmaak_f32 v13, v12, v13, 0x3e088382
	v_fmaak_f32 v13, v12, v13, 0xbeaaaa99
	v_mul_f32_e64 v13, |v19|, v13
	v_fma_f32 v29, v12, v13, |v19|
	s_or_b64 exec, exec, s[0:1]
	v_mov_b64_e32 v[12:13], v[200:201]
	v_mov_b64_e32 v[14:15], v[202:203]
	s_mov_b32 s0, 0x3f200000
	s_waitcnt vmcnt(0)
	v_add_f32_e32 v12, v8, v12
	v_cmp_nlt_f32_e64 s[0:1], |v12|, s0
	s_and_saveexec_b64 s[2:3], s[0:1]
	s_xor_b64 s[0:1], exec, s[2:3]
	s_cbranch_execz .LBB2_134
	v_add_f32_e64 v8, |v12|, |v12|
	v_mul_f32_e32 v22, 0x3fb8aa3b, v8
	s_mov_b32 s2, 0x3fb8aa3b
	v_rndne_f32_e32 v23, v22
	v_sub_f32_e32 v30, v22, v23
	v_fma_f32 v22, v8, s2, -v22
	v_fmamk_f32 v22, v8, 0x32a5705f, v22
	v_add_f32_e32 v22, v30, v22
	v_exp_f32_e32 v22, v22
	v_cvt_i32_f32_e32 v23, v23
	s_mov_b32 s2, 0xc2ce8ed0
	v_cmp_ngt_f32_e32 vcc, s2, v8
	s_mov_b32 s2, 0x42b17218
	v_ldexp_f32 v22, v22, v23
	v_cndmask_b32_e32 v22, 0, v22, vcc
	v_mov_b32_e32 v23, 0x7f800000
	v_cmp_nlt_f32_e32 vcc, s2, v8
	s_nop 1
	v_cndmask_b32_e32 v8, v23, v22, vcc
	v_add_f32_e32 v8, 1.0, v8
	v_rcp_f32_e32 v8, v8
	s_nop 0
	v_fma_f32 v22, v8, -2.0, 1.0

.LBB2_146:
	s_andn2_saveexec_b64 s[0:1], s[0:1]
	v_mul_f32_e32 v8, v15, v15
	v_mov_b32_e32 v9, 0x3ca908c9
	v_fmac_f32_e32 v9, 0xbbbac73d, v8
	v_fmaak_f32 v9, v8, v9, 0xbd5c1c4e
	v_fmaak_f32 v9, v8, v9, 0x3e088382
	v_fmaak_f32 v9, v8, v9, 0xbeaaaa99
	v_mul_f32_e64 v9, |v15|, v9
	v_fma_f32 v31, v8, v9, |v15|
	s_or_b64 exec, exec, s[0:1]
	v_mov_b64_e32 v[8:9], v[204:205]
	v_mov_b64_e32 v[10:11], v[206:207]
	s_mov_b32 s0, 0x3f200000
	s_waitcnt vmcnt(0)
	v_add_f32_e32 v8, v4, v8
	v_cmp_nlt_f32_e64 s[0:1], |v8|, s0
	s_and_saveexec_b64 s[2:3], s[0:1]
	s_xor_b64 s[0:1], exec, s[2:3]
	s_cbranch_execz .LBB2_150
	v_add_f32_e64 v4, |v8|, |v8|
	v_mul_f32_e32 v32, 0x3fb8aa3b, v4
	s_mov_b32 s2, 0x3fb8aa3b
	v_rndne_f32_e32 v33, v32
	v_sub_f32_e32 v34, v32, v33
	v_fma_f32 v32, v4, s2, -v32
	v_fmamk_f32 v32, v4, 0x32a5705f, v32
	v_add_f32_e32 v32, v34, v32
	v_exp_f32_e32 v32, v32
	v_cvt_i32_f32_e32 v33, v33
	s_mov_b32 s2, 0xc2ce8ed0
	v_cmp_ngt_f32_e32 vcc, s2, v4
	s_mov_b32 s2, 0x42b17218
	v_ldexp_f32 v32, v32, v33
	v_cndmask_b32_e32 v32, 0, v32, vcc
	v_mov_b32_e32 v33, 0x7f800000
	v_cmp_nlt_f32_e32 vcc, s2, v4
	s_nop 1
	v_cndmask_b32_e32 v4, v33, v32, vcc
	v_add_f32_e32 v4, 1.0, v4
	v_rcp_f32_e32 v4, v4
	s_nop 0
	v_fma_f32 v32, v4, -2.0, 1.0

.LBB2_162:
	s_andn2_saveexec_b64 s[0:1], s[0:1]
	v_mul_f32_e32 v4, v11, v11
	v_mov_b32_e32 v5, 0x3ca908c9
	v_fmac_f32_e32 v5, 0xbbbac73d, v4
	v_fmaak_f32 v5, v4, v5, 0xbd5c1c4e
	v_fmaak_f32 v5, v4, v5, 0x3e088382
	v_fmaak_f32 v5, v4, v5, 0xbeaaaa99
	v_mul_f32_e64 v5, |v11|, v5
	v_fma_f32 v35, v4, v5, |v11|
	s_or_b64 exec, exec, s[0:1]
	v_mov_b64_e32 v[4:5], v[208:209]
	v_mov_b64_e32 v[6:7], v[210:211]
	s_mov_b32 s0, 0x3f200000
	s_waitcnt vmcnt(0)
	v_add_f32_e32 v0, v0, v4
	v_cmp_nlt_f32_e64 s[0:1], |v0|, s0
	s_and_saveexec_b64 s[2:3], s[0:1]
	s_xor_b64 s[0:1], exec, s[2:3]
	s_cbranch_execz .LBB2_166
	v_add_f32_e64 v4, |v0|, |v0|
	v_mul_f32_e32 v16, 0x3fb8aa3b, v4
	s_mov_b32 s2, 0x3fb8aa3b
	v_rndne_f32_e32 v17, v16
	v_sub_f32_e32 v36, v16, v17
	v_fma_f32 v16, v4, s2, -v16
	v_fmamk_f32 v16, v4, 0x32a5705f, v16
	v_add_f32_e32 v16, v36, v16
	v_exp_f32_e32 v16, v16
	v_cvt_i32_f32_e32 v17, v17
	s_mov_b32 s2, 0xc2ce8ed0
	v_cmp_ngt_f32_e32 vcc, s2, v4
	s_mov_b32 s2, 0x42b17218
	v_ldexp_f32 v16, v16, v17
	v_cndmask_b32_e32 v16, 0, v16, vcc
	v_mov_b32_e32 v17, 0x7f800000
	v_cmp_nlt_f32_e32 vcc, s2, v4
	s_nop 1
	v_cndmask_b32_e32 v4, v17, v16, vcc
	v_add_f32_e32 v4, 1.0, v4
	v_rcp_f32_e32 v4, v4
	s_nop 0
	v_fma_f32 v4, v4, -2.0, 1.0
